# v90 + MLA unit-queue atomic issued before the unit-top barrier (pop latency overlaps the barrier wait)
# baseline (speedup 1.0000x reference)
; __device__ __forceinline__ void p4_mla_loop(Frame& F, const Args& A, const int qo) {
;     ...
;     for (;;) {
;         __syncthreads();
;         if (tid == 0) F.MISC[16] = __hip_atomic_fetch_add(F.ctl + CW_QUEUE + qo, 1u, RLX_AGENT);
;         __syncthreads();
;         const int it = __builtin_amdgcn_readfirstlane((int)F.MISC[16]);
.Lmla_skipA:
	s_barrier
	s_branch .LBB0_790

; __device__ __forceinline__ void p4_mla_loop(Frame& F, const Args& A, const int qo) {
;     ...
;     for (;;) {
;         __syncthreads();
;         if (tid == 0) F.MISC[16] = __hip_atomic_fetch_add(F.ctl + CW_QUEUE + qo, 1u, RLX_AGENT);
;         __syncthreads();
;         const int it = __builtin_amdgcn_readfirstlane((int)F.MISC[16]);
.LBB0_786:
	s_and_saveexec_b64 s[4:5], s[0:1]
	s_cbranch_execz .Lmla_skipA
	s_mov_b64 s[8:9], exec
	v_mbcnt_lo_u32_b32 v2, s8, 0
	v_mbcnt_hi_u32_b32 v2, s9, v2
	v_cmp_eq_u32_e32 vcc, 0, v2
	s_and_saveexec_b64 s[6:7], vcc
	s_cbranch_execz .LBB0_789
	s_bcnt1_i32_b64 s8, s[8:9]
	v_mov_b32_e32 v4, s8
	global_atomic_add v4, v3, v4, s[94:95] offset:256 sc0
.LBB0_789:
	s_or_b64 exec, exec, s[6:7]
	s_barrier
	s_waitcnt vmcnt(0)
	v_readfirstlane_b32 s6, v4
	s_nop 1
	v_add_u32_e32 v2, s6, v2
	v_readlane_b32 s6, v254, 62
	s_nop 1
	v_mov_b32_e32 v4, s6
	ds_write_b32 v4, v2
